# PEER V first half, token-start path: next batch's row loads issued before the wait for the token-start loads (counted vmcnt(16)) instead of behind a full drain
# speedup vs baseline: 1.0007x; 1.0007x over previous
.LBB0_1807:
	v_mov_b32_e32 v2, v0
	v_mov_b32_e32 v3, v0
	v_mov_b32_e32 v1, v0
	v_mov_b64_e32 v[162:163], v[2:3]
	v_mov_b64_e32 v[166:167], v[2:3]
	v_mov_b64_e32 v[154:155], v[2:3]
	v_mov_b64_e32 v[158:159], v[2:3]
	v_mov_b64_e32 v[160:161], v[0:1]
	v_mov_b64_e32 v[164:165], v[0:1]
	v_mov_b64_e32 v[152:153], v[0:1]
	v_mov_b64_e32 v[156:157], v[0:1]
.LBB0_1808:
	s_cmp_gt_i32 s57, 15
	s_cbranch_scc1 .Lpv_ts_nopf
	s_lshl_b32 s38, s59, 3
	s_waitcnt lgkmcnt(0)
	v_readlane_b32 s39, v250, s38
	s_lshl_b32 s30, s39, 10
	s_and_b32 s30, s30, 0x3fffc00
	v_lshl_add_u64 v[2:3], v[226:227], 0, s[30:31]
	s_bfe_u32 s30, s39, 0x100010
	s_lshl_b32 s30, s30, 10
	v_lshl_add_u64 v[8:9], v[226:227], 0, s[30:31]
	s_or_b32 s30, s38, 1
	v_readlane_b32 s39, v250, s30
	s_lshl_b32 s30, s39, 10
	s_and_b32 s30, s30, 0x3fffc00
	global_load_dwordx4 v[4:7], v[2:3], off
	s_nop 0
	global_load_dwordx4 v[8:11], v[8:9], off
	v_lshl_add_u64 v[2:3], v[226:227], 0, s[30:31]
	s_bfe_u32 s30, s39, 0x100010
	s_lshl_b32 s30, s30, 10
	v_lshl_add_u64 v[16:17], v[226:227], 0, s[30:31]
	s_or_b32 s30, s38, 2
	v_readlane_b32 s39, v250, s30
	s_lshl_b32 s30, s39, 10
	s_and_b32 s30, s30, 0x3fffc00
	global_load_dwordx4 v[12:15], v[2:3], off
	s_nop 0
	global_load_dwordx4 v[16:19], v[16:17], off
	v_lshl_add_u64 v[2:3], v[226:227], 0, s[30:31]
	s_bfe_u32 s30, s39, 0x100010
	s_lshl_b32 s30, s30, 10
	v_lshl_add_u64 v[24:25], v[226:227], 0, s[30:31]
	s_or_b32 s30, s38, 3
	v_readlane_b32 s39, v250, s30
	s_lshl_b32 s30, s39, 10
	s_and_b32 s30, s30, 0x3fffc00
	global_load_dwordx4 v[20:23], v[2:3], off
	s_nop 0
	global_load_dwordx4 v[24:27], v[24:25], off
	v_lshl_add_u64 v[2:3], v[226:227], 0, s[30:31]
	s_bfe_u32 s30, s39, 0x100010
	s_lshl_b32 s30, s30, 10
	v_lshl_add_u64 v[32:33], v[226:227], 0, s[30:31]
	s_or_b32 s30, s38, 4
	v_readlane_b32 s39, v250, s30
	s_lshl_b32 s30, s39, 10
	s_and_b32 s30, s30, 0x3fffc00
	global_load_dwordx4 v[28:31], v[2:3], off
	s_nop 0
	global_load_dwordx4 v[32:35], v[32:33], off
	v_lshl_add_u64 v[2:3], v[226:227], 0, s[30:31]
	s_bfe_u32 s30, s39, 0x100010
	s_lshl_b32 s30, s30, 10
	v_lshl_add_u64 v[40:41], v[226:227], 0, s[30:31]
	s_or_b32 s30, s38, 5
	v_readlane_b32 s39, v250, s30
	s_lshl_b32 s30, s39, 10
	s_and_b32 s30, s30, 0x3fffc00
	global_load_dwordx4 v[36:39], v[2:3], off
	s_nop 0
	global_load_dwordx4 v[40:43], v[40:41], off
	v_lshl_add_u64 v[2:3], v[226:227], 0, s[30:31]
	s_bfe_u32 s30, s39, 0x100010
	s_lshl_b32 s30, s30, 10
	v_lshl_add_u64 v[48:49], v[226:227], 0, s[30:31]
	s_or_b32 s30, s38, 6
	v_readlane_b32 s39, v250, s30
	s_lshl_b32 s30, s39, 10
	s_and_b32 s30, s30, 0x3fffc00
	global_load_dwordx4 v[44:47], v[2:3], off
	s_nop 0
	global_load_dwordx4 v[48:51], v[48:49], off
	v_lshl_add_u64 v[2:3], v[226:227], 0, s[30:31]
	s_bfe_u32 s30, s39, 0x100010
	s_lshl_b32 s30, s30, 10
	v_lshl_add_u64 v[56:57], v[226:227], 0, s[30:31]
	s_or_b32 s30, s38, 7
	v_readlane_b32 s38, v250, s30
	s_lshl_b32 s30, s38, 10
	s_and_b32 s30, s30, 0x3fffc00
	global_load_dwordx4 v[52:55], v[2:3], off
	s_nop 0
	global_load_dwordx4 v[56:59], v[56:57], off
	v_lshl_add_u64 v[2:3], v[226:227], 0, s[30:31]
	s_bfe_u32 s30, s38, 0x100010
	s_lshl_b32 s30, s30, 10
	v_lshl_add_u64 v[64:65], v[226:227], 0, s[30:31]
	global_load_dwordx4 v[60:63], v[2:3], off
	s_nop 0
	global_load_dwordx4 v[64:67], v[64:65], off
	s_waitcnt vmcnt(16)
	s_branch .Lpv_ts_go

.Lpv_ts_go:
	s_lshl_b32 s38, s58, 9
	s_add_i32 s38, s15, s38
	s_lshl_b32 s39, s56, 6
	s_add_i32 s38, s38, s39
	v_mov_b32_e32 v168, s38
	ds_read_b128 v[170:173], v168
